# plain bf16 proj epilogue: lane-transpose each 16-B store through ds_bpermute so 4 adjacent lanes write 64 contiguous bytes (coalesced store requests)
# speedup vs baseline: 1.0132x; 1.0017x over previous
; #define PG8_ST16(rs, b0, p, v) __builtin_amdgcn_raw_buffer_store_b128(v, rs, (int)((const char*)(p) - (const char*)(b0)), 0, 16)
; __device__ __forceinline__ unsigned cvt_pk_bf16(float lo, float hi) { unsigned r; asm volatile("v_cvt_pk_bf16_f32 %0, %1, %2" : "=v"(r) : "v"(lo), "v"(hi)); return r; }
;     __device__ __forceinline__ void operator()(const f32x4 (&acc)[2][2][4][2], const Unit& u, int wr, int wc, int fr, int fq) const {
;     ...
;         } else if (pn == 8 || pn >= 15) {
;             const int col0 = pn * BM + wc * 32 + 8 * fq;
; #pragma unroll
;             for (int ai = 0; ai < 2; ++ai)
; #pragma unroll
;                 for (int m = 0; m < 4; ++m) { bf16_t* rowp = P + (size_t)(row0 + ai * HALF + m * 16) * ldp + col0;
; #pragma unroll
;                     for (int bj = 0; bj < 2; ++bj) { const f32x4 v0 = acc[ai][bj][m][0], v1 = acc[ai][bj][m][1]; u32x4 w; w.x = cvt_pk_bf16(v0[0], v0[1]); w.y = cvt_pk_bf16(v0[2], v0[3]); w.z = cvt_pk_bf16(v1[0], v1[1]); w.w = cvt_pk_bf16(v1[2], v1[3]);
;                         PG8_ST16(rsp_, P, rowp + bj * HALF, w); } }
.LBB0_233:
	s_andn2_b64 vcc, exec, s[34:35]
	s_cbranch_vccnz .LBB0_235
	v_lshrrev_b32_e32 v176, 2, v215
	v_and_b32_e32 v177, 15, v215
	v_sub_u32_e32 v176, v176, v177
	v_add_u32_e32 v178, v164, v176
	v_and_b32_e32 v176, 3, v215
	v_lshrrev_b32_e32 v177, 4, v215
	v_sub_u32_e32 v177, v176, v177
	v_lshl_add_u32 v179, v177, 3, v196
	v_and_b32_e32 v177, 60, v215
	v_lshl_or_b32 v244, v176, 6, v177
	v_lshl_or_b32 v134, s27, 8, v179
	v_mov_b32_e32 v135, v2
	v_lshlrev_b64 v[134:135], 1, v[134:135]
	v_lshl_add_u64 v[226:227], s[20:21], 0, v[134:135]
	s_movk_i32 s36, 0x2400
	v_mad_i64_i32 v[204:205], s[34:35], v178, s36, v[226:227]
	v_cvt_pk_bf16_f32 v218, v124, v125
	v_cvt_pk_bf16_f32 v219, v126, v127
	v_cvt_pk_bf16_f32 v220, v116, v117
	v_cvt_pk_bf16_f32 v221, v118, v119
	ds_bpermute_b32 v228, v244, v218
	ds_bpermute_b32 v229, v244, v219
	ds_bpermute_b32 v230, v244, v220
	ds_bpermute_b32 v231, v244, v221
	v_cvt_pk_bf16_f32 v222, v128, v129
	v_cvt_pk_bf16_f32 v223, v130, v131
	v_cvt_pk_bf16_f32 v224, v120, v121
	v_cvt_pk_bf16_f32 v225, v122, v123
	ds_bpermute_b32 v232, v244, v222
	ds_bpermute_b32 v233, v244, v223
	ds_bpermute_b32 v234, v244, v224
	ds_bpermute_b32 v235, v244, v225
	s_waitcnt lgkmcnt(4)
	global_store_dwordx4 v[204:205], v[228:231], off
	v_or_b32_e32 v132, 16, v178
	v_mad_i64_i32 v[198:199], s[34:35], v132, s36, v[226:227]
	v_cvt_pk_bf16_f32 v218, v108, v109
	v_cvt_pk_bf16_f32 v219, v110, v111
	v_cvt_pk_bf16_f32 v220, v100, v101
	v_cvt_pk_bf16_f32 v221, v102, v103
	ds_bpermute_b32 v236, v244, v218
	ds_bpermute_b32 v237, v244, v219
	ds_bpermute_b32 v238, v244, v220
	ds_bpermute_b32 v239, v244, v221
	s_waitcnt lgkmcnt(4)
	global_store_dwordx4 v[204:205], v[232:235], off offset:256
	v_cvt_pk_bf16_f32 v222, v112, v113
	v_cvt_pk_bf16_f32 v223, v114, v115
	v_cvt_pk_bf16_f32 v224, v104, v105
	v_cvt_pk_bf16_f32 v225, v106, v107
	ds_bpermute_b32 v240, v244, v222
	ds_bpermute_b32 v241, v244, v223
	ds_bpermute_b32 v242, v244, v224
	ds_bpermute_b32 v243, v244, v225
	s_waitcnt lgkmcnt(4)
	global_store_dwordx4 v[198:199], v[236:239], off
	v_or_b32_e32 v132, 32, v178
	v_mad_i64_i32 v[204:205], s[34:35], v132, s36, v[226:227]
	v_cvt_pk_bf16_f32 v218, v92, v93
	v_cvt_pk_bf16_f32 v219, v94, v95
	v_cvt_pk_bf16_f32 v220, v84, v85
	v_cvt_pk_bf16_f32 v221, v86, v87
	ds_bpermute_b32 v228, v244, v218
	ds_bpermute_b32 v229, v244, v219
	ds_bpermute_b32 v230, v244, v220
	ds_bpermute_b32 v231, v244, v221
	s_waitcnt lgkmcnt(4)
	global_store_dwordx4 v[198:199], v[240:243], off offset:256
	v_cvt_pk_bf16_f32 v222, v96, v97
	v_cvt_pk_bf16_f32 v223, v98, v99
	v_cvt_pk_bf16_f32 v224, v88, v89
	v_cvt_pk_bf16_f32 v225, v90, v91
	ds_bpermute_b32 v232, v244, v222
	ds_bpermute_b32 v233, v244, v223
	ds_bpermute_b32 v234, v244, v224
	ds_bpermute_b32 v235, v244, v225
	s_waitcnt lgkmcnt(4)
	global_store_dwordx4 v[204:205], v[228:231], off
	v_or_b32_e32 v132, 48, v178
	v_mad_i64_i32 v[198:199], s[34:35], v132, s36, v[226:227]
	v_cvt_pk_bf16_f32 v218, v76, v77
	v_cvt_pk_bf16_f32 v219, v78, v79
	v_cvt_pk_bf16_f32 v220, v68, v69
	v_cvt_pk_bf16_f32 v221, v70, v71
	ds_bpermute_b32 v236, v244, v218
	ds_bpermute_b32 v237, v244, v219
	ds_bpermute_b32 v238, v244, v220
	ds_bpermute_b32 v239, v244, v221
	s_waitcnt lgkmcnt(4)
	global_store_dwordx4 v[204:205], v[232:235], off offset:256
	v_cvt_pk_bf16_f32 v222, v80, v81
	v_cvt_pk_bf16_f32 v223, v82, v83
	v_cvt_pk_bf16_f32 v224, v72, v73
	v_cvt_pk_bf16_f32 v225, v74, v75
	ds_bpermute_b32 v240, v244, v222
	ds_bpermute_b32 v241, v244, v223
	ds_bpermute_b32 v242, v244, v224
	ds_bpermute_b32 v243, v244, v225
	s_waitcnt lgkmcnt(4)
	global_store_dwordx4 v[198:199], v[236:239], off
	v_add_u32_e32 v132, 0x80, v178
	v_mad_i64_i32 v[204:205], s[34:35], v132, s36, v[226:227]
	v_cvt_pk_bf16_f32 v218, v60, v61
	v_cvt_pk_bf16_f32 v219, v62, v63
	v_cvt_pk_bf16_f32 v220, v52, v53
	v_cvt_pk_bf16_f32 v221, v54, v55
	ds_bpermute_b32 v228, v244, v218
	ds_bpermute_b32 v229, v244, v219
	ds_bpermute_b32 v230, v244, v220
	ds_bpermute_b32 v231, v244, v221
	s_waitcnt lgkmcnt(4)
	global_store_dwordx4 v[198:199], v[240:243], off offset:256
	v_cvt_pk_bf16_f32 v222, v64, v65
	v_cvt_pk_bf16_f32 v223, v66, v67
	v_cvt_pk_bf16_f32 v224, v56, v57
	v_cvt_pk_bf16_f32 v225, v58, v59
	ds_bpermute_b32 v232, v244, v222
	ds_bpermute_b32 v233, v244, v223
	ds_bpermute_b32 v234, v244, v224
	ds_bpermute_b32 v235, v244, v225
	s_waitcnt lgkmcnt(4)
	global_store_dwordx4 v[204:205], v[228:231], off
	v_add_u32_e32 v132, 0x90, v178
	v_mad_i64_i32 v[198:199], s[34:35], v132, s36, v[226:227]
	v_cvt_pk_bf16_f32 v218, v44, v45
	v_cvt_pk_bf16_f32 v219, v46, v47
	v_cvt_pk_bf16_f32 v220, v36, v37
	v_cvt_pk_bf16_f32 v221, v38, v39
	ds_bpermute_b32 v236, v244, v218
	ds_bpermute_b32 v237, v244, v219
	ds_bpermute_b32 v238, v244, v220
	ds_bpermute_b32 v239, v244, v221
	s_waitcnt lgkmcnt(4)
	global_store_dwordx4 v[204:205], v[232:235], off offset:256
	v_cvt_pk_bf16_f32 v222, v48, v49
	v_cvt_pk_bf16_f32 v223, v50, v51
	v_cvt_pk_bf16_f32 v224, v40, v41
	v_cvt_pk_bf16_f32 v225, v42, v43
	ds_bpermute_b32 v240, v244, v222
	ds_bpermute_b32 v241, v244, v223
	ds_bpermute_b32 v242, v244, v224
	ds_bpermute_b32 v243, v244, v225
	s_waitcnt lgkmcnt(4)
	global_store_dwordx4 v[198:199], v[236:239], off
	v_add_u32_e32 v132, 0xa0, v178
	v_mad_i64_i32 v[204:205], s[34:35], v132, s36, v[226:227]
	v_cvt_pk_bf16_f32 v218, v28, v29
	v_cvt_pk_bf16_f32 v219, v30, v31
	v_cvt_pk_bf16_f32 v220, v20, v21
	v_cvt_pk_bf16_f32 v221, v22, v23
	ds_bpermute_b32 v228, v244, v218
	ds_bpermute_b32 v229, v244, v219
	ds_bpermute_b32 v230, v244, v220
	ds_bpermute_b32 v231, v244, v221
	s_waitcnt lgkmcnt(4)
	global_store_dwordx4 v[198:199], v[240:243], off offset:256
	v_cvt_pk_bf16_f32 v222, v32, v33
	v_cvt_pk_bf16_f32 v223, v34, v35
	v_cvt_pk_bf16_f32 v224, v24, v25
	v_cvt_pk_bf16_f32 v225, v26, v27
	ds_bpermute_b32 v232, v244, v222
	ds_bpermute_b32 v233, v244, v223
	ds_bpermute_b32 v234, v244, v224
	ds_bpermute_b32 v235, v244, v225
	s_waitcnt lgkmcnt(4)
	global_store_dwordx4 v[204:205], v[228:231], off
	v_add_u32_e32 v132, 0xb0, v178
	v_mad_i64_i32 v[198:199], s[34:35], v132, s36, v[226:227]
	v_cvt_pk_bf16_f32 v218, v12, v13
	v_cvt_pk_bf16_f32 v219, v14, v15
	v_cvt_pk_bf16_f32 v220, v4, v5
	v_cvt_pk_bf16_f32 v221, v6, v7
	ds_bpermute_b32 v236, v244, v218
	ds_bpermute_b32 v237, v244, v219
	ds_bpermute_b32 v238, v244, v220
	ds_bpermute_b32 v239, v244, v221
	s_waitcnt lgkmcnt(4)
	global_store_dwordx4 v[204:205], v[232:235], off offset:256
	v_cvt_pk_bf16_f32 v222, v16, v17
	v_cvt_pk_bf16_f32 v223, v18, v19
	v_cvt_pk_bf16_f32 v224, v8, v9
	v_cvt_pk_bf16_f32 v225, v10, v11
	ds_bpermute_b32 v240, v244, v222
	ds_bpermute_b32 v241, v244, v223
	ds_bpermute_b32 v242, v244, v224
	ds_bpermute_b32 v243, v244, v225
	s_waitcnt lgkmcnt(4)
	global_store_dwordx4 v[198:199], v[236:239], off
	s_waitcnt lgkmcnt(0)
	global_store_dwordx4 v[198:199], v[240:243], off offset:256
